# v43 variant: P2/P6 next-iteration bookkeeping (stage indices, pointers, m0 values, read addresses) moved into the shadow of the fragment reads; post-burst block keeps only the k counter and the two fl
# speedup vs baseline: 1.0091x; 1.0091x over previous
.LBB0_210:
	s_barrier
	s_waitcnt lgkmcnt(7)
	v_mfma_f32_16x16x32_bf16 v[122:125], v[130:133], v[174:177], v[122:125]
	v_mfma_f32_16x16x32_bf16 v[126:129], v[134:137], v[174:177], v[126:129]
	v_mfma_f32_16x16x32_bf16 v[114:117], v[138:141], v[174:177], v[114:117]
	v_mfma_f32_16x16x32_bf16 v[110:113], v[142:145], v[174:177], v[110:113]
	s_waitcnt lgkmcnt(6)
	v_mfma_f32_16x16x32_bf16 v[106:109], v[130:133], v[170:173], v[106:109]
	v_mfma_f32_16x16x32_bf16 v[118:121], v[134:137], v[170:173], v[118:121]
	v_mfma_f32_16x16x32_bf16 v[98:101], v[138:141], v[170:173], v[98:101]
	v_mfma_f32_16x16x32_bf16 v[94:97], v[142:145], v[170:173], v[94:97]
	s_waitcnt lgkmcnt(5)
	v_mfma_f32_16x16x32_bf16 v[90:93], v[130:133], v[166:169], v[90:93]
	v_mfma_f32_16x16x32_bf16 v[102:105], v[134:137], v[166:169], v[102:105]
	v_mfma_f32_16x16x32_bf16 v[82:85], v[138:141], v[166:169], v[82:85]
	v_mfma_f32_16x16x32_bf16 v[78:81], v[142:145], v[166:169], v[78:81]
	s_waitcnt lgkmcnt(4)
	v_mfma_f32_16x16x32_bf16 v[74:77], v[130:133], v[162:165], v[74:77]
	v_mfma_f32_16x16x32_bf16 v[86:89], v[134:137], v[162:165], v[86:89]
	v_mfma_f32_16x16x32_bf16 v[70:73], v[138:141], v[162:165], v[70:73]
	v_mfma_f32_16x16x32_bf16 v[62:65], v[142:145], v[162:165], v[62:65]
	s_waitcnt lgkmcnt(3)
	v_mfma_f32_16x16x32_bf16 v[58:61], v[130:133], v[158:161], v[58:61]
	v_mfma_f32_16x16x32_bf16 v[66:69], v[134:137], v[158:161], v[66:69]
	v_mfma_f32_16x16x32_bf16 v[54:57], v[138:141], v[158:161], v[54:57]
	v_mfma_f32_16x16x32_bf16 v[46:49], v[142:145], v[158:161], v[46:49]
	s_waitcnt lgkmcnt(2)
	v_mfma_f32_16x16x32_bf16 v[42:45], v[130:133], v[154:157], v[42:45]
	v_mfma_f32_16x16x32_bf16 v[50:53], v[134:137], v[154:157], v[50:53]
	v_mfma_f32_16x16x32_bf16 v[38:41], v[138:141], v[154:157], v[38:41]
	v_mfma_f32_16x16x32_bf16 v[34:37], v[142:145], v[154:157], v[34:37]
	s_waitcnt lgkmcnt(1)
	v_mfma_f32_16x16x32_bf16 v[26:29], v[130:133], v[150:153], v[26:29]
	v_mfma_f32_16x16x32_bf16 v[30:33], v[134:137], v[150:153], v[30:33]
	v_mfma_f32_16x16x32_bf16 v[22:25], v[138:141], v[150:153], v[22:25]
	v_mfma_f32_16x16x32_bf16 v[18:21], v[142:145], v[150:153], v[18:21]
	s_waitcnt lgkmcnt(0)
	v_mfma_f32_16x16x32_bf16 v[10:13], v[130:133], v[146:149], v[10:13]
	v_mfma_f32_16x16x32_bf16 v[14:17], v[134:137], v[146:149], v[14:17]
	v_mfma_f32_16x16x32_bf16 v[6:9], v[138:141], v[146:149], v[6:9]
	v_mfma_f32_16x16x32_bf16 v[2:5], v[142:145], v[146:149], v[2:5]
	s_add_i32 s85, s85, 1
	s_cmp_gt_u32 s85, 61
	s_cselect_b64 vcc, exec, 0
	s_cmp_eq_u32 s85, 64
	s_barrier
	s_cbranch_scc1 .Lp2_exit

.Lp2_nodma:
	ds_read_b64_tr_b16 v[130:131], v192 offset:49152
	ds_read_b64_tr_b16 v[132:133], v192 offset:51200
	ds_read_b64_tr_b16 v[134:135], v193 offset:49152
	ds_read_b64_tr_b16 v[136:137], v193 offset:51200
	ds_read_b64_tr_b16 v[138:139], v194 offset:49152
	ds_read_b64_tr_b16 v[140:141], v194 offset:51200
	ds_read_b64_tr_b16 v[142:143], v195 offset:49152
	ds_read_b64_tr_b16 v[144:145], v195 offset:51200
	ds_read_b128 v[174:177], v196
	ds_read_b128 v[170:173], v196 offset:1024
	ds_read_b128 v[166:169], v196 offset:2048
	ds_read_b128 v[162:165], v196 offset:3072
	ds_read_b128 v[158:161], v196 offset:4096
	ds_read_b128 v[154:157], v196 offset:5120
	ds_read_b128 v[150:153], v196 offset:6144
	ds_read_b128 v[146:149], v196 offset:7168
	s_add_i32 s2, s86, 1
	s_cmp_lg_u32 s86, 2
	s_cselect_b32 s86, s2, 0
	s_add_i32 s2, s84, 1
	s_cmp_lg_u32 s84, 2
	s_cselect_b32 s84, s2, 0
	v_lshl_add_u64 v[180:181], v[180:181], 0, 64
	v_lshl_add_u64 v[182:183], v[182:183], 0, 64
	v_lshl_add_u64 v[184:185], v[184:185], 0, s[40:41]
	v_lshl_add_u64 v[186:187], v[186:187], 0, s[40:41]
	s_lshl_b32 s2, s84, 14
	s_add_i32 s98, s2, s70
	s_add_i32 s99, s98, 0x2000
	s_add_i32 s100, s2, s71
	s_add_i32 s101, s100, 0x2000
	s_lshl_b32 s2, s86, 14
	v_add_u32_e32 v192, s2, v178
	v_add_u32_e32 v193, s2, v189
	v_add_u32_e32 v194, s2, v190
	v_add_u32_e32 v195, s2, v191
	v_add_u32_e32 v196, s2, v188
	s_cbranch_vccnz .Lp2_tail
	s_waitcnt vmcnt(4) lgkmcnt(0)
	s_branch .LBB0_210

.LBB0_614:
	s_barrier
	s_waitcnt lgkmcnt(7)
	v_mfma_f32_16x16x32_bf16 v[126:129], v[130:133], v[174:177], v[126:129]
	v_mfma_f32_16x16x32_bf16 v[102:105], v[134:137], v[174:177], v[102:105]
	v_mfma_f32_16x16x32_bf16 v[70:73], v[138:141], v[174:177], v[70:73]
	v_mfma_f32_16x16x32_bf16 v[38:41], v[142:145], v[174:177], v[38:41]
	s_waitcnt lgkmcnt(6)
	v_mfma_f32_16x16x32_bf16 v[122:125], v[130:133], v[170:173], v[122:125]
	v_mfma_f32_16x16x32_bf16 v[94:97], v[134:137], v[170:173], v[94:97]
	v_mfma_f32_16x16x32_bf16 v[62:65], v[138:141], v[170:173], v[62:65]
	v_mfma_f32_16x16x32_bf16 v[30:33], v[142:145], v[170:173], v[30:33]
	s_waitcnt lgkmcnt(5)
	v_mfma_f32_16x16x32_bf16 v[118:121], v[130:133], v[166:169], v[118:121]
	v_mfma_f32_16x16x32_bf16 v[86:89], v[134:137], v[166:169], v[86:89]
	v_mfma_f32_16x16x32_bf16 v[54:57], v[138:141], v[166:169], v[54:57]
	v_mfma_f32_16x16x32_bf16 v[22:25], v[142:145], v[166:169], v[22:25]
	s_waitcnt lgkmcnt(4)
	v_mfma_f32_16x16x32_bf16 v[114:117], v[130:133], v[162:165], v[114:117]
	v_mfma_f32_16x16x32_bf16 v[82:85], v[134:137], v[162:165], v[82:85]
	v_mfma_f32_16x16x32_bf16 v[50:53], v[138:141], v[162:165], v[50:53]
	v_mfma_f32_16x16x32_bf16 v[18:21], v[142:145], v[162:165], v[18:21]
	s_waitcnt lgkmcnt(3)
	v_mfma_f32_16x16x32_bf16 v[110:113], v[130:133], v[158:161], v[110:113]
	v_mfma_f32_16x16x32_bf16 v[78:81], v[134:137], v[158:161], v[78:81]
	v_mfma_f32_16x16x32_bf16 v[46:49], v[138:141], v[158:161], v[46:49]
	v_mfma_f32_16x16x32_bf16 v[14:17], v[142:145], v[158:161], v[14:17]
	s_waitcnt lgkmcnt(2)
	v_mfma_f32_16x16x32_bf16 v[106:109], v[130:133], v[154:157], v[106:109]
	v_mfma_f32_16x16x32_bf16 v[74:77], v[134:137], v[154:157], v[74:77]
	v_mfma_f32_16x16x32_bf16 v[42:45], v[138:141], v[154:157], v[42:45]
	v_mfma_f32_16x16x32_bf16 v[10:13], v[142:145], v[154:157], v[10:13]
	s_waitcnt lgkmcnt(1)
	v_mfma_f32_16x16x32_bf16 v[98:101], v[130:133], v[150:153], v[98:101]
	v_mfma_f32_16x16x32_bf16 v[66:69], v[134:137], v[150:153], v[66:69]
	v_mfma_f32_16x16x32_bf16 v[34:37], v[138:141], v[150:153], v[34:37]
	v_mfma_f32_16x16x32_bf16 v[6:9], v[142:145], v[150:153], v[6:9]
	s_waitcnt lgkmcnt(0)
	v_mfma_f32_16x16x32_bf16 v[90:93], v[130:133], v[146:149], v[90:93]
	v_mfma_f32_16x16x32_bf16 v[58:61], v[134:137], v[146:149], v[58:61]
	v_mfma_f32_16x16x32_bf16 v[26:29], v[138:141], v[146:149], v[26:29]
	v_mfma_f32_16x16x32_bf16 v[2:5], v[142:145], v[146:149], v[2:5]
	s_add_i32 s61, s61, 1
	s_cmp_gt_u32 s61, 61
	s_cselect_b64 vcc, exec, 0
	s_cmp_eq_u32 s61, 64
	s_barrier
	s_cbranch_scc1 .Lp6_exit

.Lp6_nodma:
	ds_read_b64_tr_b16 v[130:131], v192 offset:49152
	ds_read_b64_tr_b16 v[132:133], v192 offset:51200
	ds_read_b64_tr_b16 v[134:135], v193 offset:49152
	ds_read_b64_tr_b16 v[136:137], v193 offset:51200
	ds_read_b64_tr_b16 v[138:139], v194 offset:49152
	ds_read_b64_tr_b16 v[140:141], v194 offset:51200
	ds_read_b64_tr_b16 v[142:143], v195 offset:49152
	ds_read_b64_tr_b16 v[144:145], v195 offset:51200
	ds_read_b128 v[174:177], v196
	ds_read_b128 v[170:173], v196 offset:1024
	ds_read_b128 v[166:169], v196 offset:2048
	ds_read_b128 v[162:165], v196 offset:3072
	ds_read_b128 v[158:161], v196 offset:4096
	ds_read_b128 v[154:157], v196 offset:5120
	ds_read_b128 v[150:153], v196 offset:6144
	ds_read_b128 v[146:149], v196 offset:7168
	s_add_i32 s2, s62, 1
	s_cmp_lg_u32 s62, 2
	s_cselect_b32 s62, s2, 0
	s_add_i32 s2, s60, 1
	s_cmp_lg_u32 s60, 2
	s_cselect_b32 s60, s2, 0
	v_lshl_add_u64 v[180:181], v[180:181], 0, 64
	v_lshl_add_u64 v[182:183], v[182:183], 0, 64
	v_lshl_add_u64 v[184:185], v[184:185], 0, s[20:21]
	v_lshl_add_u64 v[186:187], v[186:187], 0, s[20:21]
	s_lshl_b32 s2, s60, 14
	s_add_i32 s98, s2, s58
	s_add_i32 s99, s98, 0x2000
	s_add_i32 s100, s2, s59
	s_add_i32 s101, s100, 0x2000
	s_lshl_b32 s2, s62, 14
	v_add_u32_e32 v192, s2, v178
	v_add_u32_e32 v193, s2, v189
	v_add_u32_e32 v194, s2, v190
	v_add_u32_e32 v195, s2, v191
	v_add_u32_e32 v196, s2, v188
	s_cbranch_vccnz .Lp6_tail
	s_waitcnt vmcnt(4) lgkmcnt(0)
	s_branch .LBB0_614
